# v47 + packed->scalar fp32 split: hipcc's SLP-packed v_pk_add_f32 row-sum adds in the sub-head-1 softmax of both diff-attention loops replaced by scalar v_add_f32 pairs
# speedup vs baseline: 1.0068x; 1.0068x over previous
.LBB0_200:
	v_add_u32_e32 v212, v0, v231
	v_add_u32_e32 v213, v0, v232
	v_add_u32_e32 v0, v0, v233
	s_waitcnt lgkmcnt(0)
	v_mfma_f32_32x32x16_bf16 v[160:175], v[248:251], v[192:195], v[160:175]
	ds_read_b128 v[248:251], v212 offset:8192
	v_mfma_f32_32x32x16_bf16 v[144:159], v[236:239], v[192:195], v[144:159]
	ds_read_b128 v[236:239], v213
	v_mfma_f32_32x32x16_bf16 v[160:175], v[244:247], v[196:199], v[160:175]
	ds_read_b128 v[244:247], v213 offset:8192
	s_waitcnt lgkmcnt(2)
	v_mfma_f32_32x32x16_bf16 v[144:159], v[248:251], v[196:199], v[144:159]
	ds_read_b128 v[248:251], v0
	s_waitcnt lgkmcnt(2)
	v_mfma_f32_32x32x16_bf16 v[160:175], v[236:239], v[200:203], v[160:175]
	ds_read_b128 v[236:239], v0 offset:8192
	s_waitcnt lgkmcnt(2)
	v_mfma_f32_32x32x16_bf16 v[144:159], v[244:247], v[200:203], v[144:159]
	v_add_f32_e32 v0, v14, v15
	v_add_f32_e32 v235, v235, v0
	s_waitcnt lgkmcnt(1)
	v_mfma_f32_32x32x16_bf16 v[160:175], v[248:251], v[204:207], v[160:175]
	s_waitcnt lgkmcnt(0)
	v_mfma_f32_32x32x16_bf16 v[144:159], v[236:239], v[204:207], v[144:159]
	s_nop 10
	v_exp_f32_e32 v14, v160
	v_exp_f32_e32 v160, v161
	v_exp_f32_e32 v164, v164
	v_exp_f32_e32 v15, v168
	v_exp_f32_e32 v161, v169
	v_exp_f32_e32 v162, v162
	v_exp_f32_e32 v220, v163
	v_exp_f32_e32 v166, v166
	s_nop 4
	v_exp_f32_e32 v246, v148
	v_exp_f32_e32 v148, v165
	v_exp_f32_e32 v248, v149
	v_exp_f32_e32 v165, v172
	v_exp_f32_e32 v149, v173
	v_exp_f32_e32 v250, v150
	v_exp_f32_e32 v150, v167
	v_exp_f32_e32 v163, v170
	v_exp_f32_e32 v167, v174
	v_exp_f32_e32 v252, v151
	v_exp_f32_e32 v221, v171
	v_exp_f32_e32 v151, v175
	v_exp_f32_e32 v144, v144
	v_exp_f32_e32 v212, v145
	v_exp_f32_e32 v145, v152
	v_exp_f32_e32 v247, v156
	v_exp_f32_e32 v244, v147
	v_exp_f32_e32 v213, v153
	v_exp_f32_e32 v147, v154
	v_exp_f32_e32 v245, v155
	v_exp_f32_e32 v249, v157
	v_add_f32_e32 v152, v14, v160
	v_add_f32_e32 v153, v15, v161
	v_add_f32_e32 v154, v164, v148
	v_add_f32_e32 v155, v165, v149
	v_exp_f32_e32 v146, v146
	v_exp_f32_e32 v251, v158
	v_add_f32_e32 v152, v162, v152
	v_add_f32_e32 v153, v163, v153
	v_add_f32_e32 v154, v166, v154
	v_add_f32_e32 v155, v167, v155
	v_exp_f32_e32 v253, v159
	v_add_f32_e32 v152, v220, v152
	v_add_f32_e32 v153, v221, v153
	v_add_f32_e32 v154, v150, v154
	v_add_f32_e32 v155, v151, v155
	v_add_f32_e32 v152, v144, v152
	v_add_f32_e32 v153, v145, v153
	v_add_f32_e32 v154, v246, v154
	v_add_f32_e32 v155, v247, v155
	v_add_f32_e32 v152, v212, v152
	v_add_f32_e32 v153, v213, v153
	v_add_f32_e32 v154, v248, v154
	v_add_f32_e32 v155, v249, v155
	v_add_f32_e32 v152, v146, v152
	v_add_f32_e32 v153, v147, v153
	v_add_f32_e32 v154, v250, v154
	v_add_f32_e32 v155, v251, v155
	v_add_f32_e32 v152, v244, v152
	v_add_f32_e32 v153, v245, v153
	v_add_f32_e32 v154, v252, v154
	v_add_f32_e32 v155, v253, v155
	v_cvt_pk_bf16_f32 v156, v14, v160
	v_add_f32_e32 v152, v152, v154
	v_add_f32_e32 v153, v153, v155
	v_cvt_pk_bf16_f32 v157, v162, v220
	v_add_f32_e32 v152, v152, v153
	v_mov_b32_e32 v153, v152
	v_cvt_pk_bf16_f32 v158, v164, v148
	v_mov_b32_e32 v0, v152
	s_nop 1
	v_permlane32_swap_b32_e32 v152, v0
	v_add_f32_e32 v0, v152, v0
	v_cvt_pk_bf16_f32 v159, v166, v150
	v_cvt_pk_bf16_f32 v152, v15, v161
	v_cvt_pk_bf16_f32 v153, v163, v221
	v_cvt_pk_bf16_f32 v154, v165, v149
	v_cvt_pk_bf16_f32 v155, v167, v151
	v_cvt_pk_bf16_f32 v148, v144, v212
	v_cvt_pk_bf16_f32 v149, v146, v244
	v_cvt_pk_bf16_f32 v150, v246, v248
	v_cvt_pk_bf16_f32 v151, v250, v252
	v_cvt_pk_bf16_f32 v144, v145, v213
	v_cvt_pk_bf16_f32 v145, v147, v245
	v_cvt_pk_bf16_f32 v146, v247, v249
	v_cvt_pk_bf16_f32 v147, v251, v253
	v_add_f32_e32 v234, v234, v0
	v_permlane32_swap_b32_e32 v156, v158
	v_permlane32_swap_b32_e32 v157, v159
	v_permlane32_swap_b32_e32 v152, v154
	v_permlane32_swap_b32_e32 v153, v155
	v_permlane32_swap_b32_e32 v148, v150
	v_permlane32_swap_b32_e32 v149, v151
	v_permlane32_swap_b32_e32 v144, v146
	v_permlane32_swap_b32_e32 v145, v147
	s_add_i32 s42, s49, 0x4000
	s_cmpk_lg_u32 s49, 0xc000
	s_cselect_b32 s42, s42, 0
	s_add_i32 s43, s90, 0x4000
	s_cmpk_lg_u32 s90, 0xc000
	s_cselect_b32 s90, s43, 0
	s_add_u32 s40, s40, 0x60000
	s_addc_u32 s41, s41, 0
	s_addk_i32 s71, 0x100
	s_add_i32 s73, s73, 64
	s_add_i32 s86, s86, 1
	s_cmpk_eq_i32 s71, 0x4000
	s_cbranch_scc1 .LBB0_202
	s_mov_b32 s44, s49
	s_mov_b32 s49, s42
	s_cmpk_eq_i32 s71, 0x3f00
	s_mov_b64 s[42:43], -1
	s_cbranch_scc0 .LBB0_191
	s_branch .LBB0_185

.LBB0_205:
	v_add_u32_e32 v219, v212, v232
	v_add_u32_e32 v212, v212, v233
	s_waitcnt lgkmcnt(0)
	v_mfma_f32_32x32x16_bf16 v[144:159], v[248:251], v[192:195], v[144:159]
	ds_read_b128 v[248:251], v219
	v_mfma_f32_32x32x16_bf16 v[160:175], v[236:239], v[192:195], v[160:175]
	ds_read_b128 v[236:239], v219 offset:8192
	v_mfma_f32_32x32x16_bf16 v[144:159], v[240:243], v[196:199], v[144:159]
	ds_read_b128 v[240:243], v212
	v_mfma_f32_32x32x16_bf16 v[160:175], v[244:247], v[196:199], v[160:175]
	ds_read_b128 v[244:247], v212 offset:8192
	s_waitcnt lgkmcnt(3)
	v_mfma_f32_32x32x16_bf16 v[144:159], v[248:251], v[200:203], v[144:159]
	s_waitcnt lgkmcnt(2)
	v_mfma_f32_32x32x16_bf16 v[160:175], v[236:239], v[200:203], v[160:175]
	v_add_f32_e32 v212, v213, v218
	v_add_f32_e32 v235, v235, v212
	s_waitcnt lgkmcnt(1)
	v_mfma_f32_32x32x16_bf16 v[144:159], v[240:243], v[204:207], v[144:159]
	s_waitcnt lgkmcnt(0)
	v_mfma_f32_32x32x16_bf16 v[160:175], v[244:247], v[204:207], v[160:175]
	s_nop 10
	v_exp_f32_e32 v212, v144
	v_exp_f32_e32 v218, v145
	v_exp_f32_e32 v242, v148
	v_exp_f32_e32 v244, v149
	v_exp_f32_e32 v213, v152
	v_exp_f32_e32 v219, v153
	v_exp_f32_e32 v243, v156
	v_exp_f32_e32 v245, v157
	v_exp_f32_e32 v236, v146
	v_exp_f32_e32 v150, v150
	v_exp_f32_e32 v248, v151
	v_exp_f32_e32 v237, v154
	v_exp_f32_e32 v151, v158
	v_exp_f32_e32 v238, v147
	v_exp_f32_e32 v239, v155
	v_exp_f32_e32 v249, v159
	v_exp_f32_e32 v160, v160
	v_exp_f32_e32 v220, v161
	v_exp_f32_e32 v164, v164
	v_exp_f32_e32 v246, v165
	v_exp_f32_e32 v161, v168
	v_exp_f32_e32 v165, v172
	v_exp_f32_e32 v221, v169
	v_exp_f32_e32 v247, v173
	v_add_f32_e32 v144, v212, v218
	v_add_f32_e32 v145, v213, v219
	v_add_f32_e32 v146, v242, v244
	v_add_f32_e32 v147, v243, v245
	v_exp_f32_e32 v162, v162
	v_exp_f32_e32 v240, v163
	v_exp_f32_e32 v166, v166
	v_exp_f32_e32 v250, v167
	v_exp_f32_e32 v163, v170
	v_exp_f32_e32 v167, v174
	v_add_f32_e32 v144, v236, v144
	v_add_f32_e32 v145, v237, v145
	v_add_f32_e32 v146, v150, v146
	v_add_f32_e32 v147, v151, v147
	v_exp_f32_e32 v241, v171
	v_exp_f32_e32 v251, v175
	v_add_f32_e32 v144, v238, v144
	v_add_f32_e32 v145, v239, v145
	v_add_f32_e32 v146, v248, v146
	v_add_f32_e32 v147, v249, v147
	v_add_f32_e32 v144, v160, v144
	v_add_f32_e32 v145, v161, v145
	v_add_f32_e32 v146, v164, v146
	v_add_f32_e32 v147, v165, v147
	v_add_f32_e32 v144, v220, v144
	v_add_f32_e32 v145, v221, v145
	v_add_f32_e32 v146, v246, v146
	v_add_f32_e32 v147, v247, v147
	v_add_f32_e32 v144, v162, v144
	v_add_f32_e32 v145, v163, v145
	v_add_f32_e32 v146, v166, v146
	v_add_f32_e32 v147, v167, v147
	v_add_f32_e32 v144, v240, v144
	v_add_f32_e32 v145, v241, v145
	v_add_f32_e32 v146, v250, v146
	v_add_f32_e32 v147, v251, v147
	v_cvt_pk_bf16_f32 v148, v213, v219
	v_add_f32_e32 v144, v144, v146
	v_add_f32_e32 v145, v145, v147
	v_cvt_pk_bf16_f32 v146, v242, v244
	v_add_f32_e32 v144, v144, v145
	v_mov_b32_e32 v145, v144
	v_cvt_pk_bf16_f32 v147, v150, v248
	v_mov_b32_e32 v145, v144
	s_nop 1
	v_permlane32_swap_b32_e32 v144, v145
	v_add_f32_e32 v144, v144, v145
	v_add_f32_e32 v234, v234, v144
	v_cvt_pk_bf16_f32 v144, v212, v218
	v_cvt_pk_bf16_f32 v145, v236, v238
	v_cvt_pk_bf16_f32 v149, v237, v239
	v_cvt_pk_bf16_f32 v150, v243, v245
	v_cvt_pk_bf16_f32 v151, v151, v249
	v_cvt_pk_bf16_f32 v152, v160, v220
	v_cvt_pk_bf16_f32 v153, v162, v240
	v_cvt_pk_bf16_f32 v154, v164, v246
	v_cvt_pk_bf16_f32 v155, v166, v250
	v_cvt_pk_bf16_f32 v156, v161, v221
	v_cvt_pk_bf16_f32 v157, v163, v241
	v_cvt_pk_bf16_f32 v158, v165, v247
	v_cvt_pk_bf16_f32 v159, v167, v251
	v_permlane32_swap_b32_e32 v144, v146
	v_permlane32_swap_b32_e32 v145, v147
	v_permlane32_swap_b32_e32 v148, v150
	v_permlane32_swap_b32_e32 v149, v151
	v_permlane32_swap_b32_e32 v152, v154
	v_permlane32_swap_b32_e32 v153, v155
	v_permlane32_swap_b32_e32 v156, v158
	v_permlane32_swap_b32_e32 v157, v159
	s_waitcnt lgkmcnt(0)
	v_add_u32_e32 v212, s56, v224
	ds_read_b64_tr_b16 v[160:161], v212 offset:0
	ds_read_b64_tr_b16 v[162:163], v212 offset:0x800
	ds_read_b64_tr_b16 v[164:165], v212 offset:0x200
	ds_read_b64_tr_b16 v[166:167], v212 offset:0xa00
	ds_read_b64_tr_b16 v[168:169], v212 offset:0x400
	ds_read_b64_tr_b16 v[170:171], v212 offset:0xc00
	ds_read_b64_tr_b16 v[172:173], v212 offset:0x600
	ds_read_b64_tr_b16 v[174:175], v212 offset:0xe00
	s_waitcnt lgkmcnt(4)
	s_nop 0
	v_mfma_f32_32x32x16_bf16 v[112:127], v[208:211], v[160:163], v[112:127]
	v_mfma_f32_32x32x16_bf16 v[96:111], v[208:211], v[164:167], v[96:111]
	v_mfma_f32_32x32x16_bf16 v[128:143], v[144:147], v[160:163], v[128:143]
	v_mfma_f32_32x32x16_bf16 v[80:95], v[144:147], v[164:167], v[80:95]
	ds_read_b64_tr_b16 v[160:161], v212 offset:0x1000
	ds_read_b64_tr_b16 v[162:163], v212 offset:0x1800
	ds_read_b64_tr_b16 v[164:165], v212 offset:0x1200
	ds_read_b64_tr_b16 v[166:167], v212 offset:0x1a00
	s_waitcnt lgkmcnt(4)
	v_mfma_f32_32x32x16_bf16 v[64:79], v[208:211], v[168:171], v[64:79]
	v_mfma_f32_32x32x16_bf16 v[48:63], v[208:211], v[172:175], v[48:63]
	v_mfma_f32_32x32x16_bf16 v[32:47], v[144:147], v[168:171], v[32:47]
	v_mfma_f32_32x32x16_bf16 v[16:31], v[144:147], v[172:175], v[16:31]
	ds_read_b64_tr_b16 v[144:145], v212 offset:0x1400
	ds_read_b64_tr_b16 v[146:147], v212 offset:0x1c00
	ds_read_b64_tr_b16 v[168:169], v212 offset:0x1600
	ds_read_b64_tr_b16 v[170:171], v212 offset:0x1e00
	s_waitcnt lgkmcnt(4)
	v_mfma_f32_32x32x16_bf16 v[112:127], v[10:13], v[160:163], v[112:127]
	v_mfma_f32_32x32x16_bf16 v[96:111], v[10:13], v[164:167], v[96:111]
	v_mfma_f32_32x32x16_bf16 v[128:143], v[148:151], v[160:163], v[128:143]
	v_mfma_f32_32x32x16_bf16 v[80:95], v[148:151], v[164:167], v[80:95]
	ds_read_b64_tr_b16 v[160:161], v212 offset:0x2000
	ds_read_b64_tr_b16 v[162:163], v212 offset:0x2800
	ds_read_b64_tr_b16 v[164:165], v212 offset:0x2200
	ds_read_b64_tr_b16 v[166:167], v212 offset:0x2a00
	s_waitcnt lgkmcnt(4)
	v_mfma_f32_32x32x16_bf16 v[64:79], v[10:13], v[144:147], v[64:79]
	v_mfma_f32_32x32x16_bf16 v[48:63], v[10:13], v[168:171], v[48:63]
	v_mfma_f32_32x32x16_bf16 v[32:47], v[148:151], v[144:147], v[32:47]
	v_mfma_f32_32x32x16_bf16 v[16:31], v[148:151], v[168:171], v[16:31]
	ds_read_b64_tr_b16 v[10:11], v212 offset:0x2400
	ds_read_b64_tr_b16 v[12:13], v212 offset:0x2c00
	ds_read_b64_tr_b16 v[144:145], v212 offset:0x2600
	ds_read_b64_tr_b16 v[146:147], v212 offset:0x2e00
	s_waitcnt lgkmcnt(4)
	v_mfma_f32_32x32x16_bf16 v[112:127], v[6:9], v[160:163], v[112:127]
	v_mfma_f32_32x32x16_bf16 v[96:111], v[6:9], v[164:167], v[96:111]
	v_mfma_f32_32x32x16_bf16 v[128:143], v[152:155], v[160:163], v[128:143]
	v_mfma_f32_32x32x16_bf16 v[80:95], v[152:155], v[164:167], v[80:95]
	ds_read_b64_tr_b16 v[148:149], v212 offset:0x3000
	ds_read_b64_tr_b16 v[150:151], v212 offset:0x3800
	ds_read_b64_tr_b16 v[160:161], v212 offset:0x3200
	ds_read_b64_tr_b16 v[162:163], v212 offset:0x3a00
	s_waitcnt lgkmcnt(4)
	v_mfma_f32_32x32x16_bf16 v[64:79], v[6:9], v[10:13], v[64:79]
	v_mfma_f32_32x32x16_bf16 v[48:63], v[6:9], v[144:147], v[48:63]
	v_mfma_f32_32x32x16_bf16 v[32:47], v[152:155], v[10:13], v[32:47]
	v_mfma_f32_32x32x16_bf16 v[16:31], v[152:155], v[144:147], v[16:31]
	ds_read_b64_tr_b16 v[6:7], v212 offset:0x3400
	ds_read_b64_tr_b16 v[8:9], v212 offset:0x3c00
	ds_read_b64_tr_b16 v[10:11], v212 offset:0x3600
	ds_read_b64_tr_b16 v[12:13], v212 offset:0x3e00
	s_waitcnt lgkmcnt(4)
	v_mfma_f32_32x32x16_bf16 v[112:127], v[2:5], v[148:151], v[112:127]
	v_mfma_f32_32x32x16_bf16 v[96:111], v[2:5], v[160:163], v[96:111]
	v_mfma_f32_32x32x16_bf16 v[128:143], v[156:159], v[148:151], v[128:143]
	v_mfma_f32_32x32x16_bf16 v[80:95], v[156:159], v[160:163], v[80:95]
	s_waitcnt lgkmcnt(0)
	v_mfma_f32_32x32x16_bf16 v[64:79], v[2:5], v[6:9], v[64:79]
	v_mfma_f32_32x32x16_bf16 v[48:63], v[2:5], v[10:13], v[48:63]
	v_mfma_f32_32x32x16_bf16 v[32:47], v[156:159], v[6:9], v[32:47]
	v_mfma_f32_32x32x16_bf16 v[16:31], v[156:159], v[10:13], v[16:31]
	s_add_i32 s42, s56, 0x4000
	s_cmpk_lg_u32 s56, 0xc000
	s_cselect_b32 s56, s42, 0
	s_add_i32 s42, s90, 0x4000
	s_cmpk_lg_u32 s90, 0xc000
	s_cselect_b32 s90, s42, 0
	s_add_u32 s40, s40, 0x60000
	s_addc_u32 s41, s41, 0
	s_addk_i32 s73, 0x100
	s_add_i32 s72, s72, 64
	s_add_i32 s71, s71, 1
	s_cmpk_eq_i32 s73, 0x4000
	s_cbranch_scc1 .LBB0_220
